# P2 inner loop loop-edge edits: interior-tile first MFMA and no-rescale path fall through, masked variants and rescale block out of line, single conditional back edge
# speedup vs baseline: 1.0041x; 1.0041x over previous
.LBB0_325:
	v_add_u32_e32 v3, 0, v206
	ds_read_b64_tr_b16 v[162:163], v3 offset:55296
	ds_read_b64_tr_b16 v[164:165], v3 offset:56320
	ds_read_b64_tr_b16 v[4:5], v3 offset:57344
	ds_read_b64_tr_b16 v[6:7], v3 offset:58368
	v_add_u32_e32 v3, 0, v193
	ds_read_b64_tr_b16 v[12:13], v3 offset:55296
	ds_read_b64_tr_b16 v[14:15], v3 offset:56320
	ds_read_b64_tr_b16 v[8:9], v3 offset:57344
	ds_read_b64_tr_b16 v[10:11], v3 offset:58368
	s_cmp_lg_u32 s69, s70
	s_cbranch_scc0 .Lp2_mask_last
	s_cmp_lg_u32 s7, s70
	s_cbranch_scc0 .Lp2_mask_first
	s_waitcnt lgkmcnt(11)
	v_mfma_f32_32x32x16_bf16 v[98:113], v[178:181], v[138:141], 0
.LBB0_333:
	s_waitcnt lgkmcnt(10)
	v_mfma_f32_32x32x16_bf16 v[98:113], v[174:177], v[142:145], v[98:113]
	s_waitcnt lgkmcnt(9)
	v_mfma_f32_32x32x16_bf16 v[98:113], v[170:173], v[146:149], v[98:113]
	s_waitcnt lgkmcnt(8)
	v_mfma_f32_32x32x16_bf16 v[98:113], v[166:169], v[150:153], v[98:113]
	s_nop 11
	ds_read_b128 v[178:181], v192 offset:4608
	ds_read_b128 v[174:177], v192 offset:4624
	ds_read_b128 v[170:173], v192 offset:4640
	ds_read_b128 v[166:169], v192 offset:4656
	v_max_f32_e32 v3, v99, v99
	v_max_f32_e32 v16, v98, v98
	v_max_f32_e32 v3, v16, v3
	v_max3_f32 v3, v3, v100, v101
	v_max3_f32 v3, v3, v102, v103
	v_max3_f32 v3, v3, v104, v105
	v_max3_f32 v3, v3, v106, v107
	v_max3_f32 v3, v3, v108, v109
	v_max3_f32 v3, v3, v110, v111
	v_max3_f32 v3, v3, v112, v113
	v_mov_b32_e32 v16, v3
	s_nop 1
	v_permlane32_swap_b32_e32 v3, v16
	v_max_f32_e32 v16, v16, v16
	v_max_f32_e32 v3, v3, v3
	v_max_f32_e32 v3, v3, v16
	v_add_f32_e32 v16, 0x41000000, v205
	v_cmp_gt_f32_e32 vcc, v3, v16
	s_cbranch_vccnz .Lp2_rescale
.LBB0_335:
	v_sub_f32_e32 v3, v98, v205
	v_sub_f32_e32 v98, v101, v205
	v_sub_f32_e32 v16, v99, v205
	v_exp_f32_e32 v99, v98
	v_sub_f32_e32 v98, v102, v205
	v_sub_f32_e32 v17, v100, v205
	v_exp_f32_e32 v100, v98
	v_sub_f32_e32 v98, v103, v205
	v_exp_f32_e32 v101, v98
	v_sub_f32_e32 v98, v104, v205
	v_exp_f32_e32 v102, v98
	v_sub_f32_e32 v98, v105, v205
	v_exp_f32_e32 v103, v98
	v_sub_f32_e32 v98, v106, v205
	v_exp_f32_e32 v104, v98
	v_sub_f32_e32 v98, v107, v205
	v_exp_f32_e32 v105, v98
	v_sub_f32_e32 v98, v108, v205
	v_exp_f32_e32 v106, v98
	v_sub_f32_e32 v98, v109, v205
	v_exp_f32_e32 v3, v3
	v_exp_f32_e32 v16, v16
	v_exp_f32_e32 v17, v17
	v_exp_f32_e32 v107, v98
	v_sub_f32_e32 v98, v110, v205
	v_exp_f32_e32 v108, v98
	v_sub_f32_e32 v98, v111, v205
	v_exp_f32_e32 v109, v98
	v_sub_f32_e32 v98, v112, v205
	v_exp_f32_e32 v110, v98
	v_sub_f32_e32 v98, v113, v205
	v_exp_f32_e32 v111, v98
	v_cvt_pk_bf16_f32 v98, v3, v16
	v_cvt_pk_bf16_f32 v99, v17, v99
	v_cvt_pk_bf16_f32 v100, v100, v101
	v_cvt_pk_bf16_f32 v101, v102, v103
	s_mov_b32 s29, s28
	s_mov_b32 s30, s28
	s_waitcnt lgkmcnt(2)
	v_mfma_f32_32x32x16_bf16 v[82:97], v[12:15], v[98:101], v[82:97]
	s_mov_b32 s31, s28
	v_mov_b64_e32 v[12:13], s[28:29]
	v_mov_b64_e32 v[14:15], s[30:31]
	v_cvt_pk_bf16_f32 v102, v104, v105
	v_cvt_pk_bf16_f32 v103, v106, v107
	v_cvt_pk_bf16_f32 v104, v108, v109
	v_cvt_pk_bf16_f32 v105, v110, v111
	v_mfma_f32_32x32x16_bf16 v[66:81], v[162:165], v[98:101], v[66:81]
	s_add_i32 s8, s70, 1
	s_add_i32 s9, s70, -4
	v_add_u32_e32 v192, 0x1200, v192
	v_add_u32_e32 v193, 0x1000, v193
	v_add_u32_e32 v206, 0x1000, v206
	s_cmp_ge_i32 s9, s7
	v_mfma_f32_32x32x16_bf16 v[50:65], v[12:15], v[98:101], v[50:65]
	v_mfma_f32_32x32x16_bf16 v[66:81], v[4:7], v[102:105], v[66:81]
	s_waitcnt lgkmcnt(0)
	v_mfma_f32_32x32x16_bf16 v[82:97], v[8:11], v[102:105], v[82:97]
	v_mfma_f32_32x32x16_bf16 v[50:65], v[12:15], v[102:105], v[50:65]
	s_mov_b32 s70, s8
	s_cbranch_scc0 .LBB0_325
	s_branch .LBB0_338
.Lp2_mask_last:
	s_waitcnt lgkmcnt(11)
	v_mfma_f32_32x32x16_bf16 v[98:113], v[178:181], v[138:141], v[18:33]
	s_branch .LBB0_333
.Lp2_mask_first:
	s_waitcnt lgkmcnt(11)
	v_mfma_f32_32x32x16_bf16 v[98:113], v[178:181], v[138:141], v[34:49]
	s_branch .LBB0_333
.Lp2_rescale:
	v_max_f32_e32 v3, v3, v3
	v_max_f32_e32 v16, v205, v205
	v_max_f32_e32 v3, v16, v3
	v_sub_f32_e32 v16, v205, v3
	v_exp_f32_e32 v16, v16
	v_mov_b32_e32 v205, v3
	v_mul_f32_e32 v50, v50, v16
	v_pk_mul_f32 v[80:81], v[80:81], v[16:17] op_sel_hi:[1,0]
	v_pk_mul_f32 v[78:79], v[78:79], v[16:17] op_sel_hi:[1,0]
	v_pk_mul_f32 v[76:77], v[76:77], v[16:17] op_sel_hi:[1,0]
	v_pk_mul_f32 v[74:75], v[74:75], v[16:17] op_sel_hi:[1,0]
	v_pk_mul_f32 v[72:73], v[72:73], v[16:17] op_sel_hi:[1,0]
	v_pk_mul_f32 v[70:71], v[70:71], v[16:17] op_sel_hi:[1,0]
	v_pk_mul_f32 v[68:69], v[68:69], v[16:17] op_sel_hi:[1,0]
	v_pk_mul_f32 v[66:67], v[66:67], v[16:17] op_sel_hi:[1,0]
	v_pk_mul_f32 v[96:97], v[96:97], v[16:17] op_sel_hi:[1,0]
	v_pk_mul_f32 v[94:95], v[94:95], v[16:17] op_sel_hi:[1,0]
	v_pk_mul_f32 v[92:93], v[92:93], v[16:17] op_sel_hi:[1,0]
	v_pk_mul_f32 v[90:91], v[90:91], v[16:17] op_sel_hi:[1,0]
	v_pk_mul_f32 v[88:89], v[88:89], v[16:17] op_sel_hi:[1,0]
	v_pk_mul_f32 v[86:87], v[86:87], v[16:17] op_sel_hi:[1,0]
	v_pk_mul_f32 v[84:85], v[84:85], v[16:17] op_sel_hi:[1,0]
	v_pk_mul_f32 v[82:83], v[82:83], v[16:17] op_sel_hi:[1,0]
	s_branch .LBB0_335
